# speedup vs baseline: 1.0156x; 1.0156x over previous
.LBB0_283:
	s_or_b64 exec, exec, s[0:1]
	s_waitcnt vmcnt(2)
	v_lshrrev_b32_e32 v4, 4, v160
	s_lshl_b32 s0, s78, 5
	v_or_b32_e32 v165, s0, v4
	v_mov_b32_e32 v4, 0x24400
	s_add_i32 s69, s33, 33
	v_lshl_or_b32 v169, v72, 2, v4
	v_mul_u32_u24_e32 v4, 10, v160
	s_cmp_gt_i32 s77, 8
	s_cselect_b64 s[18:19], -1, 0
	s_cmp_gt_i32 s77, 10
	v_lshlrev_b32_e32 v12, 2, v4
	v_mov_b32_e32 v13, 0
	v_or_b32_e32 v164, 0x100, v160
	v_cvt_f64_f32_e32 v[10:11], v5
	v_mov_b32_e32 v5, 0x10000
	s_cselect_b64 s[20:21], -1, 0
	s_cmp_gt_i32 s77, 12
	v_lshl_add_u64 v[14:15], s[48:49], 0, v[12:13]
	v_lshlrev_b32_e32 v4, 9, v70
	v_lshlrev_b32_e32 v12, 2, v70
	v_lshl_or_b32 v67, v160, 2, v5
	v_lshl_or_b32 v69, v164, 2, v5
	s_cselect_b64 s[22:23], -1, 0
	v_add3_u32 v172, v4, s3, v75
	v_lshl_add_u64 v[4:5], s[60:61], 0, v[12:13]
	s_add_i32 s24, s24, s3
	v_lshl_add_u64 v[40:41], v[4:5], 0, 64
	v_add_u32_e32 v4, s24, v75
	v_mov_b32_e32 v5, v13
	v_lshlrev_b64 v[4:5], 11, v[4:5]
	s_waitcnt vmcnt(1)
	v_cmp_gt_f32_e32 vcc, 0, v161
	v_or_b32_e32 v4, v4, v12
	v_lshrrev_b32_e32 v6, 4, v164
	v_cndmask_b32_e64 v167, 0, 1.0, vcc
	s_waitcnt vmcnt(0)
	v_cmp_gt_f32_e32 vcc, 0, v162
	s_mov_b64 s[10:11], 0x2800
	s_lshl_b32 s70, s68, 16
	v_lshl_add_u64 v[4:5], s[72:73], 0, v[4:5]
	v_mov_b32_e32 v12, v13
	s_mov_b32 s26, 0x3f7d73e7
	s_mov_b32 s28, 0xa37fcc69
	s_mov_b32 s34, 0x3f779b79
	s_mov_b32 s36, 0x3d064869
	v_or_b32_e32 v166, s0, v6
	v_cndmask_b32_e64 v168, 0, 1.0, vcc
	v_cmp_gt_u32_e64 s[0:1], 32, v73
	v_lshl_add_u32 v170, v73, 5, s33
	v_lshl_add_u64 v[34:35], v[14:15], 0, s[10:11]
	s_bitset1_b32 s70, 21
	v_lshlrev_b32_e32 v171, 3, v70
	v_lshl_add_u64 v[42:43], v[4:5], 0, 64
	s_mov_b64 s[38:39], 0
	v_mov_b64_e32 v[44:45], 0
	s_mov_b64 s[24:25], 0
	s_mov_b32 s27, 0x3d8414e8
	s_mov_b32 s29, 0x3fee7078
	s_mov_b32 s3, 0xf000
	s_mov_b64 s[30:31], 0x80
	s_mov_b32 s35, 0x3f7383c5
	s_mov_b32 s37, 0x3d47c3ae
	s_mov_b32 s71, 0xffff
	v_mov_b32_e32 v47, 0x3f6f7d63
	v_bfrev_b32_e32 v173, 1
	v_mov_b32_e32 v174, 0x2f0
	v_mov_b32_e32 v175, 0x26c10
	s_mov_b64 s[40:41], 0
	s_mov_b64 s[44:45], 0
	v_mov_b32_e32 v176, 0
	v_mov_b64_e32 v[36:37], 0
	v_mov_b64_e32 v[6:7], 0
	v_mov_b64_e32 v[48:49], 0
	v_mov_b64_e32 v[38:39], 0
	v_mov_b64_e32 v[4:5], 0
	v_mov_b32_e32 v177, 0
	v_mov_b64_e32 v[50:51], v[12:13]
	v_mov_b64_e32 v[56:57], v[12:13]
	v_mov_b64_e32 v[52:53], v[12:13]
	v_mov_b64_e32 v[58:59], v[12:13]
	v_mov_b32_e32 v54, v13
	v_mov_b32_e32 v55, v13
	v_mul_f32_e32 v218, v9, v18
	v_mul_f32_e32 v219, v131, v19
	v_mul_f32_e32 v220, v134, v20
	v_mul_f32_e32 v221, v137, v21
	v_mul_f32_e32 v222, v140, v22
	v_mul_f32_e32 v223, v143, v23
	v_mul_f32_e32 v224, v146, v24
	v_mul_f32_e32 v225, v150, v25
	v_mul_f32_e32 v226, v121, v26
	v_mul_f32_e32 v227, v122, v27
	v_mov_b32_e32 v250, 0
	v_add_u16_e32 v208, v250, v159
	v_add_u16_e32 v209, v250, v158
	v_add_u16_e32 v210, v250, v157
	v_add_u16_e32 v211, v250, v156
	v_add_u16_e32 v212, v250, v155
	v_add_u16_e32 v213, v250, v154
	v_add_u16_e32 v214, v250, v153
	v_add_u16_e32 v215, v250, v149
	v_add_u16_e32 v216, v250, v128
	v_add_u16_e32 v217, v250, v127
	s_and_saveexec_b64 s[82:83], s[42:43]
	v_lshlrev_b32_e32 v208, 7, v165
	v_lshlrev_b32_e32 v210, 7, v166
	v_mov_b32_e32 v209, 0x100000
	v_mov_b32_e32 v211, 0x100000
	s_mov_b64 exec, s[82:83]
	s_branch .LBB0_288

.LBB0_288:
	s_waitcnt lgkmcnt(0)
	s_barrier
	s_and_saveexec_b64 s[10:11], s[42:43]
	s_xor_b64 s[56:57], exec, s[10:11]
	s_cbranch_execz .LBB0_304
	v_and_b32_e32 v212, 3, v177
	v_mad_u32_u24 v213, v212, v209, v208
	v_mad_u32_u24 v214, v212, v211, v210
	global_load_dword v182, v213, s[66:67] sc1
	global_load_dword v183, v214, s[66:67] sc1
	v_cmp_eq_u32_e64 s[10:11], 0, v177
	v_cmp_ne_u32_e32 vcc, 0, v177
	s_and_saveexec_b64 s[12:13], vcc
	s_cbranch_execz .LBB0_291
	v_mul_f32_e32 v60, v161, v59
	v_fma_f32 v46, v167, v52, 1.0
	v_mov_b32_e32 v61, v53
	v_pk_mul_f32 v[52:53], v[60:61], v[46:47]
	v_add_u32_e32 v12, -1, v177
	v_pk_fma_f32 v[52:53], v[58:59], s[26:27], v[52:53]
	v_cvt_f64_f32_e32 v[58:59], v59
	v_fmac_f64_e32 v[58:59], s[28:29], v[44:45]
	v_cvt_f64_f32_e32 v[44:45], v57
	v_mul_f32_e32 v62, v162, v57
	v_fma_f32 v50, v168, v50, 1.0
	v_mov_b32_e32 v63, v51
	v_mov_b32_e32 v51, v47
	v_fmac_f64_e32 v[44:45], s[28:29], v[48:49]
	v_cmp_eq_u32_e32 vcc, s33, v12
	v_pk_mul_f32 v[50:51], v[62:63], v[50:51]
	v_mov_b64_e32 v[48:49], v[44:45]
	v_cndmask_b32_e32 v39, v39, v45, vcc
	v_cndmask_b32_e32 v38, v38, v44, vcc
	v_cndmask_b32_e32 v37, v37, v59, vcc
	v_cndmask_b32_e32 v36, v36, v58, vcc
	v_cmp_eq_u32_e32 vcc, s69, v177
	v_pk_fma_f32 v[50:51], v[56:57], s[26:27], v[50:51]
	s_nop 0
	v_cndmask_b32_e32 v5, v5, v45, vcc
	v_cndmask_b32_e32 v4, v4, v44, vcc
	v_cndmask_b32_e32 v7, v7, v59, vcc
	v_cndmask_b32_e32 v6, v6, v58, vcc
	v_mov_b64_e32 v[44:45], v[58:59]

.LBB0_293:
	s_or_b64 exec, exec, s[12:13]
	v_add_f32_e32 v216, 1.0, v52
	v_add_f32_e32 v217, 1.0, v50
	v_lshlrev_b32_e32 v215, 9, v177
	v_cmp_neq_f32_e32 vcc, 0, v216
	v_and_b32_e32 v215, 0x1e00, v215
	v_or_b32_e32 v250, v215, v160
	v_cndmask_b32_e32 v216, v173, v216, vcc
	v_cmp_neq_f32_e32 vcc, 0, v217
	v_or_b32_e32 v251, v215, v164
	v_lshlrev_b32_e32 v250, 3, v250
	v_cndmask_b32_e32 v217, v173, v217, vcc
	v_lshlrev_b32_e32 v251, 3, v251
	s_waitcnt vmcnt(0)
	v_mov_b32_e32 v64, v182
	v_mov_b32_e32 v46, v183
	s_xor_b64 s[50:51], s[44:45], -1
	v_add_u32_e32 v12, 1, v177
	s_mov_b64 s[12:13], -1
	s_and_saveexec_b64 s[48:49], s[50:51]
	s_cbranch_execz .LBB0_303
	v_lshrrev_b32_e32 v65, 20, v64
	v_cmp_eq_u32_e32 vcc, v65, v12
	v_lshrrev_b32_e32 v65, 20, v46
	v_cmp_eq_u32_e64 s[12:13], v65, v12
	s_and_b64 s[12:13], vcc, s[12:13]
	s_nop 0
	v_cndmask_b32_e64 v65, 0, 1, s[12:13]
	v_cmp_ne_u32_e32 vcc, 0, v65
	s_cmp_eq_u64 vcc, exec
	s_mov_b64 s[12:13], 0
	s_cbranch_scc1 .LBB0_302
	v_lshlrev_b32_e32 v72, 13, v177
	v_and_b32_e32 v72, 0x6000, v72
	v_add_u32_e32 v65, v72, v166
	v_add_u32_e32 v72, v72, v165
	v_mov_b32_e32 v73, 0
	v_lshlrev_b64 v[56:57], 7, v[72:73]
	v_mov_b32_e32 v72, v65
	v_lshl_add_u64 v[56:57], s[66:67], 0, v[56:57]
	v_lshlrev_b64 v[60:61], 7, v[72:73]
	v_mov_b32_e32 v72, v213
	v_lshl_add_u64 v[60:61], s[66:67], 0, v[60:61]
	v_lshl_add_u64 v[58:59], s[66:67], 0, v[72:73]
	v_mov_b32_e32 v72, v214
	s_nop 0
	v_lshl_add_u64 v[62:63], s[66:67], 0, v[72:73]
	s_mov_b32 s60, 0

.LBB0_303:
	s_or_b64 exec, exec, s[48:49]
	v_lshrrev_b32_e32 v57, v70, v64
	v_lshrrev_b32_e32 v65, v70, v46
	v_bfe_i32 v60, v57, 0, 1
	v_bfe_i32 v62, v65, 0, 1
	v_and_b32_e32 v60, v60, v216
	v_and_b32_e32 v62, v62, v217
	ds_write2_b32 v250, v60, v53 offset1:1
	ds_write2_b32 v251, v62, v51 offset1:1
	v_and_b32_e32 v59, 1, v57
	v_and_b32_e32 v57, 1, v65
	v_cvt_f32_ubyte0_e32 v59, v59
	v_cvt_f32_ubyte0_e32 v57, v57
	v_mov_b32_e32 v56, v50
	v_mov_b32_e32 v58, v52
	s_cmp_eq_u64 s[10:11], 0
	s_cbranch_scc1 .Lmy_rx_nt0
	v_bfe_u32 v60, v46, 16, 4
	v_bfe_u32 v61, v64, 16, 4
	v_cmp_eq_u32_e64 s[48:49], s68, v60
	v_cmp_eq_u32_e64 s[50:51], s68, v61
	v_lshlrev_b32_e32 v60, 2, v165
	v_lshlrev_b32_e32 v61, 2, v166
	v_add_u32_e32 v60, 0x400000, v60
	v_add_u32_e32 v61, 0x400000, v61
	v_cndmask_b32_e64 v208, v208, v60, s[50:51]
	v_cndmask_b32_e64 v210, v210, v61, s[48:49]
	v_mov_b32_e32 v60, 0x8000
	v_cndmask_b32_e64 v209, v209, v60, s[50:51]
	v_cndmask_b32_e64 v211, v211, v60, s[48:49]
	s_branch .Lmy_rx_end
.Lmy_rx_nt0:
	s_mov_b64 s[48:49], s[38:39]
	s_mov_b64 s[50:51], s[40:41]
.Lmy_rx_end:
.LBB0_304:
	s_andn2_saveexec_b64 s[56:57], s[56:57]
	s_cbranch_execz .LBB0_287
	v_add_u32_e32 v178, 1, v177
	v_lshlrev_b32_e32 v12, 4, v178
	v_cmp_ne_u32_e64 s[10:11], 47, v177
	s_and_b64 vcc, exec, s[6:7]
	v_lshlrev_b32_e32 v181, 12, v177
	v_cndmask_b32_e64 v12, v174, v12, s[10:11]
	v_lshl_add_u32 v12, v12, 2, v169
	ds_read_b32 v179, v12
	s_cbranch_vccnz .LBB0_313
	v_add_u32_e32 v12, 0xf000, v181
	v_add_u32_e32 v46, 0xe000, v181
	v_add_u32_e32 v60, 0xc000, v181
	v_and_or_b32 v182, v60, s3, v171
	v_and_or_b32 v183, v46, s3, v171
	v_and_or_b32 v184, v12, s3, v171
	v_mov_b32_e32 v180, 0
	s_mov_b32 s60, 0
	v_mov_b64_e32 v[60:61], v[42:43]
	v_mov_b64_e32 v[62:63], v[40:41]
	v_mov_b32_e32 v12, v172
	s_branch .LBB0_308

.LBB0_313:
	s_cbranch_execz .LBB0_318
	s_andn2_b64 vcc, exec, s[18:19]
	s_cbranch_vccnz .Lmy_rd8
	ds_read_b64 v[244:245], v216
	ds_read_b64 v[246:247], v217
.Lmy_rd8:
	ds_read_b64 v[228:229], v208
	ds_read_b64 v[230:231], v209
	ds_read_b64 v[232:233], v210
	ds_read_b64 v[234:235], v211
	ds_read_b64 v[236:237], v212
	ds_read_b64 v[238:239], v213
	ds_read_b64 v[240:241], v214
	ds_read_b64 v[242:243], v215
	s_waitcnt lgkmcnt(7)
	v_fma_f32 v180, v228, v218, 0
	s_waitcnt lgkmcnt(6)
	v_fmac_f32_e32 v180, v230, v219
	s_waitcnt lgkmcnt(5)
	v_fmac_f32_e32 v180, v232, v220
	s_waitcnt lgkmcnt(4)
	v_fmac_f32_e32 v180, v234, v221
	s_waitcnt lgkmcnt(3)
	v_fmac_f32_e32 v180, v236, v222
	s_waitcnt lgkmcnt(2)
	v_fmac_f32_e32 v180, v238, v223
	s_waitcnt lgkmcnt(1)
	v_fmac_f32_e32 v180, v240, v224
	s_waitcnt lgkmcnt(0)
	v_fmac_f32_e32 v180, v242, v225
	s_cbranch_vccnz .LBB0_318
	v_fmac_f32_e32 v180, v244, v226
	v_fmac_f32_e32 v180, v246, v227
	s_andn2_b64 vcc, exec, s[20:21]
	s_cbranch_vccnz .LBB0_318
	v_and_b32_e32 v12, 0xf000, v181
	v_add_u16_e32 v46, v12, v120
	ds_read_b64 v[60:61], v46
	v_add_u16_e32 v46, v12, v119
	ds_read_b64 v[62:63], v46
	v_mul_f32_e32 v64, v112, v28
	s_andn2_b64 vcc, exec, s[22:23]
	s_waitcnt lgkmcnt(1)
	v_mul_f32_e32 v46, v115, v61
	v_cmp_class_f32_e64 s[58:59], v60, 64
	v_fma_f32 v28, v46, v54, v28
	v_fmac_f32_e32 v180, v60, v64
	v_cndmask_b32_e64 v46, -v117, v173, s[58:59]
	v_fmac_f32_e32 v28, v46, v55
	v_mul_f32_e32 v46, v113, v29
	s_waitcnt lgkmcnt(0)
	v_fmac_f32_e32 v180, v62, v46
	v_mul_f32_e32 v46, v116, v63
	v_cmp_class_f32_e64 s[58:59], v62, 64
	v_fma_f32 v29, v46, v54, v29
	v_med3_f32 v28, v28, v93, 0
	v_cndmask_b32_e64 v46, -v118, v173, s[58:59]
	v_fmac_f32_e32 v29, v46, v55
	v_med3_f32 v29, v29, v94, 0
	s_cbranch_vccnz .LBB0_318
	v_add_u16_e32 v46, v12, v114
	v_add_u16_e32 v62, v12, v111
	v_add_u16_e32 v64, v12, v17
	v_add_u16_e32 v12, v12, v8
	ds_read_b64 v[60:61], v46
	ds_read_b64 v[62:63], v62
	ds_read_b64 v[64:65], v64
	ds_read_b64 v[72:73], v12
	v_mul_f32_e32 v12, v100, v30
	s_waitcnt lgkmcnt(3)
	v_fmac_f32_e32 v180, v60, v12
	v_mul_f32_e32 v12, v103, v61
	v_cmp_class_f32_e64 s[58:59], v60, 64
	v_fma_f32 v12, v12, v54, v30
	s_nop 0
	v_cndmask_b32_e64 v30, -v107, v173, s[58:59]
	v_fmac_f32_e32 v12, v30, v55
	v_med3_f32 v30, v12, v95, 0
	v_mul_f32_e32 v12, v101, v31
	s_waitcnt lgkmcnt(2)
	v_fmac_f32_e32 v180, v62, v12
	v_mul_f32_e32 v12, v104, v63
	v_cmp_class_f32_e64 s[58:59], v62, 64
	v_fma_f32 v12, v12, v54, v31
	s_nop 0
	v_cndmask_b32_e64 v31, -v108, v173, s[58:59]
	v_fmac_f32_e32 v12, v31, v55
	v_med3_f32 v31, v12, v96, 0
	v_mul_f32_e32 v12, v102, v32
	s_waitcnt lgkmcnt(1)
	v_fmac_f32_e32 v180, v64, v12
	v_mul_f32_e32 v12, v105, v65
	v_cmp_class_f32_e64 s[58:59], v64, 64
	v_fma_f32 v12, v12, v54, v32
	s_nop 0
	v_cndmask_b32_e64 v32, -v109, v173, s[58:59]
	v_fmac_f32_e32 v12, v32, v55
	v_med3_f32 v32, v12, v97, 0
	v_mul_f32_e32 v12, v16, v33
	s_waitcnt lgkmcnt(0)
	v_fmac_f32_e32 v180, v72, v12
	v_mul_f32_e32 v12, v106, v73
	v_cmp_class_f32_e64 s[58:59], v72, 64
	v_fmac_f32_e32 v33, v12, v54
	s_nop 0
	v_cndmask_b32_e64 v12, -v110, v173, s[58:59]
	v_fmac_f32_e32 v33, v12, v55
	v_med3_f32 v33, v33, v99, 0
.LBB0_318:
	v_mul_f32_e32 v250, v129, v229
	v_cmp_class_f32_e64 s[82:83], v228, 64
	v_add_f32_dpp v12, v180, v180 row_ror:8 row_mask:0xf bank_mask:0xf bound_ctrl:1
	v_mov_b32_e32 v61, v13
	v_cndmask_b32_e64 v46, v176, 5, s[16:17]
	v_mul_f32_e32 v251, v132, v231
	v_cmp_class_f32_e64 s[84:85], v230, 64
	v_add_f32_dpp v12, v12, v12 row_ror:4 row_mask:0xf bank_mask:0xf bound_ctrl:1
	s_mov_b64 s[60:61], s[16:17]
	v_fma_f32 v18, v250, v54, v18
	v_fma_f32 v19, v251, v54, v19
	v_cndmask_b32_e64 v250, -v130, v173, s[82:83]
	v_add_f32_dpp v60, v12, v12 row_ror:2 row_mask:0xf bank_mask:0xf bound_ctrl:1
	v_mov_b32_e32 v12, 48
	v_cndmask_b32_e64 v251, -v133, v173, s[84:85]
	v_fmac_f32_e32 v18, v250, v55
	v_fmac_f32_e32 v19, v251, v55
	v_mov_b32_dpp v61, v60 row_ror:1 row_mask:0xf bank_mask:0xf
	s_and_saveexec_b64 s[58:59], s[10:11]
	s_cbranch_execz .LBB0_286
	v_med3_f32 v18, v18, v71, 0
	v_med3_f32 v19, v19, v81, 0
	v_add_f32_e32 v12, v60, v61
	v_cvt_f64_f32_e32 v[248:249], v12
	v_mul_f32_e32 v218, v9, v18
	v_mul_f32_e32 v219, v131, v19
	v_mul_f32_e32 v250, v135, v233
	v_fmac_f64_e32 v[248:249], v[0:1], v[10:11]
	v_cmp_gt_i32_e32 vcc, 1, v46
	v_mov_b32_e32 v12, 0
	v_cmp_class_f32_e64 s[82:83], v232, 64
	v_mul_f32_e32 v251, v138, v235
	v_cmp_class_f32_e64 s[84:85], v234, 64
	v_fma_f32 v20, v250, v54, v20
	v_cndmask_b32_e32 v1, 0, v249, vcc
	v_cndmask_b32_e32 v0, 0, v248, vcc
	s_waitcnt lgkmcnt(0)
	v_cvt_f64_f32_e32 v[248:249], v179
	v_fma_f32 v21, v251, v54, v21
	v_cndmask_b32_e64 v250, -v136, v173, s[82:83]
	v_cndmask_b32_e64 v251, -v139, v173, s[84:85]
	v_add_f64 v[0:1], v[0:1], v[248:249]
	v_fmac_f32_e32 v20, v250, v55
	v_fmac_f32_e32 v21, v251, v55
	v_med3_f32 v20, v20, v85, 0
	v_med3_f32 v21, v21, v86, 0
	v_cmp_le_f64_e32 vcc, 1.0, v[0:1]
	v_mul_f32_e32 v220, v134, v20
	v_mul_f32_e32 v221, v137, v21
	v_mul_f32_e32 v250, v141, v237
	v_cmp_class_f32_e64 s[82:83], v236, 64
	s_lshr_b32 s11, vcc_lo, 15
	s_and_b32 s10, vcc_lo, 1
	s_and_b32 s11, s11, 2
	s_or_b32 s60, s11, s10
	s_lshr_b64 s[10:11], vcc, 30
	s_and_b32 s10, s10, 4
	s_lshr_b32 s11, vcc_hi, 13
	s_or_b32 s10, s60, s10
	s_and_b32 s11, s11, 8
	s_or_b32 s10, s10, s11
	v_lshlrev_b32_e64 v248, v163, s10
	s_and_saveexec_b64 s[10:11], s[4:5]
	v_and_b32_e32 v12, 3, v178
	v_lshl_or_b32 v12, v12, 2, v175
	v_or_b32_e32 v249, 0x10000, v248
	ds_add_rtn_u32 v12, v12, v249
	s_or_b64 exec, exec, s[10:11]
	v_mul_f32_e32 v251, v144, v239
	v_cmp_class_f32_e64 s[84:85], v238, 64
	v_fma_f32 v22, v250, v54, v22
	v_fma_f32 v23, v251, v54, v23
	v_cndmask_b32_e64 v250, -v142, v173, s[82:83]
	v_cndmask_b32_e64 v251, -v145, v173, s[84:85]
	v_fmac_f32_e32 v22, v250, v55
	v_fmac_f32_e32 v23, v251, v55
	v_med3_f32 v22, v22, v87, 0
	v_med3_f32 v23, v23, v88, 0
	v_mul_f32_e32 v222, v140, v22
	v_mul_f32_e32 v223, v143, v23
	v_mul_f32_e32 v250, v147, v241
	v_cmp_class_f32_e64 s[82:83], v240, 64
	v_mul_f32_e32 v251, v151, v243
	v_cmp_class_f32_e64 s[84:85], v242, 64
	v_fma_f32 v24, v250, v54, v24
	v_fma_f32 v25, v251, v54, v25
	v_cndmask_b32_e64 v250, -v148, v173, s[82:83]
	v_cndmask_b32_e64 v251, -v152, v173, s[84:85]
	v_fmac_f32_e32 v24, v250, v55
	v_fmac_f32_e32 v25, v251, v55
	v_med3_f32 v24, v24, v89, 0
	v_med3_f32 v25, v25, v90, 0
	v_mul_f32_e32 v224, v146, v24
	v_mul_f32_e32 v225, v150, v25
	v_lshlrev_b32_e32 v250, 12, v178
	v_and_b32_e32 v250, 0xf000, v250
	v_add_u16_e32 v208, v250, v159
	v_add_u16_e32 v209, v250, v158
	v_add_u16_e32 v210, v250, v157
	v_add_u16_e32 v211, v250, v156
	v_add_u16_e32 v212, v250, v155
	v_add_u16_e32 v213, v250, v154
	v_add_u16_e32 v214, v250, v153
	v_add_u16_e32 v215, v250, v149
	s_cmp_eq_u64 s[18:19], 0
	s_cbranch_scc1 .Lmy_no89
	v_mul_f32_e32 v250, v123, v245
	v_cmp_class_f32_e64 s[82:83], v244, 64
	v_mul_f32_e32 v251, v124, v247
	v_cmp_class_f32_e64 s[84:85], v246, 64
	v_fma_f32 v26, v250, v54, v26
	v_fma_f32 v27, v251, v54, v27
	v_cndmask_b32_e64 v250, -v125, v173, s[82:83]
	v_cndmask_b32_e64 v251, -v126, v173, s[84:85]
	v_fmac_f32_e32 v26, v250, v55
	v_fmac_f32_e32 v27, v251, v55
	v_med3_f32 v26, v26, v91, 0
	v_med3_f32 v27, v27, v92, 0
	v_mul_f32_e32 v226, v121, v26
	v_mul_f32_e32 v227, v122, v27
	v_lshlrev_b32_e32 v250, 12, v178
	v_and_b32_e32 v250, 0xf000, v250
	v_add_u16_e32 v216, v250, v128
	v_add_u16_e32 v217, v250, v127
.Lmy_no89:
	s_waitcnt lgkmcnt(0)
	v_readfirstlane_b32 s60, v12
	s_and_b32 s10, s60, 0xffff0000
	s_cmp_lg_u32 s10, 0x30000
	s_cbranch_scc1 .LBB0_285
	s_and_saveexec_b64 s[10:11], s[0:1]
	s_cbranch_execz .LBB0_324
	v_lshl_add_u32 v12, v177, 20, s70
	v_add_u32_e32 v248, s60, v248
	v_and_or_b32 v60, v248, s71, v12
	v_lshlrev_b32_e32 v12, 3, v178
	v_and_or_b32 v12, v12, 24, s75
	v_lshl_add_u32 v12, v12, 10, v170
	v_lshl_add_u64 v[248:249], v[12:13], 2, s[14:15]
	global_store_dword v[248:249], v60, off sc0
	v_lshlrev_b64 v[248:249], 7, v[12:13]
	v_lshl_add_u64 v[248:249], s[66:67], 0, v[248:249]
	global_store_dword v[248:249], v60, off sc1

	.amdhsa_kernel _Z10snn_kernel6Params
		.amdhsa_group_segment_fixed_size 159008
		.amdhsa_private_segment_fixed_size 0
		.amdhsa_kernarg_size 360
		.amdhsa_user_sgpr_count 2
		.amdhsa_user_sgpr_dispatch_ptr 0
		.amdhsa_user_sgpr_queue_ptr 0
		.amdhsa_user_sgpr_kernarg_segment_ptr 1
		.amdhsa_user_sgpr_dispatch_id 0
		.amdhsa_user_sgpr_kernarg_preload_length 0
		.amdhsa_user_sgpr_kernarg_preload_offset 0
		.amdhsa_user_sgpr_private_segment_size 0
		.amdhsa_uses_dynamic_stack 0
		.amdhsa_enable_private_segment 0
		.amdhsa_system_sgpr_workgroup_id_x 1
		.amdhsa_system_sgpr_workgroup_id_y 0
		.amdhsa_system_sgpr_workgroup_id_z 0
		.amdhsa_system_sgpr_workgroup_info 0
		.amdhsa_system_vgpr_workitem_id 2
		.amdhsa_next_free_vgpr 252
		.amdhsa_next_free_sgpr 96
		.amdhsa_accum_offset 252
		.amdhsa_reserve_vcc 1
		.amdhsa_float_round_mode_32 0
		.amdhsa_float_round_mode_16_64 0
		.amdhsa_float_denorm_mode_32 3
		.amdhsa_float_denorm_mode_16_64 3
		.amdhsa_dx10_clamp 1
		.amdhsa_ieee_mode 1
		.amdhsa_fp16_overflow 0
		.amdhsa_tg_split 0
		.amdhsa_exception_fp_ieee_invalid_op 0
		.amdhsa_exception_fp_denorm_src 0
		.amdhsa_exception_fp_ieee_div_zero 0
		.amdhsa_exception_fp_ieee_overflow 0
		.amdhsa_exception_fp_ieee_underflow 0
		.amdhsa_exception_fp_ieee_inexact 0
		.amdhsa_exception_int_div_zero 0
	.end_amdhsa_kernel

amdhsa.kernels:
  - .agpr_count:     0
    .args:
      - .offset:         0
        .size:           104
        .value_kind:     by_value
      - .offset:         104
        .size:           4
        .value_kind:     hidden_block_count_x
      - .offset:         108
        .size:           4
        .value_kind:     hidden_block_count_y
      - .offset:         112
        .size:           4
        .value_kind:     hidden_block_count_z
      - .offset:         116
        .size:           2
        .value_kind:     hidden_group_size_x
      - .offset:         118
        .size:           2
        .value_kind:     hidden_group_size_y
      - .offset:         120
        .size:           2
        .value_kind:     hidden_group_size_z
      - .offset:         122
        .size:           2
        .value_kind:     hidden_remainder_x
      - .offset:         124
        .size:           2
        .value_kind:     hidden_remainder_y
      - .offset:         126
        .size:           2
        .value_kind:     hidden_remainder_z
      - .offset:         144
        .size:           8
        .value_kind:     hidden_global_offset_x
      - .offset:         152
        .size:           8
        .value_kind:     hidden_global_offset_y
      - .offset:         160
        .size:           8
        .value_kind:     hidden_global_offset_z
      - .offset:         168
        .size:           2
        .value_kind:     hidden_grid_dims
    .group_segment_fixed_size: 159008
    .kernarg_segment_align: 8
    .kernarg_segment_size: 360
    .language:       OpenCL C
    .language_version:
      - 2
      - 0
    .max_flat_workgroup_size: 512
    .name:           _Z10snn_kernel6Params
    .private_segment_fixed_size: 0
    .sgpr_count:     88
    .sgpr_spill_count: 0
    .symbol:         _Z10snn_kernel6Params.kd
    .uniform_work_group_size: 1
    .uses_dynamic_stack: false
    .vgpr_count:     252
    .vgpr_spill_count: 0
    .wavefront_size: 64
